# final norm phase: next trip's row loads issued before this trip's compute and stores (software prefetch into staging registers), counted wait at loop end
# speedup vs baseline: 1.0056x; 1.0056x over previous
; __device__ __forceinline__ void phase_final(const bf16* H, float* out, const float* gain, int gw, int NGW, int lane) {
;     constexpr int NR = 4;
;     f32x4 gv[2][2];
; #pragma unroll
;     for (int j = 0; j < 2; ++j) { gv[j][0] = ((const f32x4*)gain)[2 * lane + 128 * j]; gv[j][1] = ((const f32x4*)gain)[2 * lane + 128 * j + 1]; }
;     for (int m0 = gw * NR; m0 < NTOK; m0 += NGW * NR) { u32x4 v[NR][2];
; #pragma unroll
;         for (int r = 0; r < NR; ++r)
; #pragma unroll
;             for (int j = 0; j < 2; ++j) v[r][j] = ((const u32x4*)(H + (size_t)(m0 + r) * DM))[lane + 64 * j];
; #pragma unroll
;         for (int r = 0; r < NR; ++r) { const float rstd = rsqrtf(wave_sum(ss_u4(v[r][0]) + ss_u4(v[r][1])) * (1.f / DM) + EPS);
.LBB0_1264:
	s_mov_b64 s[0:1], s[66:67]
	s_load_dword s0, s[0:1], 0x138
	s_waitcnt lgkmcnt(0)
	s_cmp_lt_i32 s0, 46
	s_cbranch_scc0 .LBB0_1269
	s_mov_b64 s[0:1], s[66:67]
	s_load_dword s0, s[0:1], 0x13c
	s_waitcnt lgkmcnt(0)
	s_cmp_lt_i32 s0, 46
	s_cbranch_scc1 .LBB0_1269
	s_lshl_b32 s0, s68, 3
	v_mbcnt_lo_u32_b32 v0, -1, 0
	v_mbcnt_hi_u32_b32 v0, -1, v0
	s_add_i32 s0, s0, s69
	v_add_u32_e32 v0, s70, v0
	s_cmpk_gt_i32 s0, 0x3fff
	s_cbranch_scc1 .LBB0_1269
	s_load_dwordx4 s[8:11], s[66:67], 0x120
	s_load_dwordx2 s[2:3], s[66:67], 0x130
	s_waitcnt vmcnt(0)
	v_and_b32_e32 v20, 63, v0
	v_lshlrev_b32_e32 v16, 5, v20
	s_lshl_b32 s6, s65, 5
	s_waitcnt lgkmcnt(0)
	global_load_dwordx4 v[0:3], v16, s[8:9] offset:16
	global_load_dwordx4 v[4:7], v16, s[8:9]
	global_load_dwordx4 v[8:11], v16, s[8:9] offset:2064
	global_load_dwordx4 v[12:15], v16, s[8:9] offset:2048
	s_lshl_b32 s8, s0, 2
	s_ashr_i32 s9, s8, 31
	s_lshl_b64 s[0:1], s[8:9], 12
	s_add_u32 s0, s10, s0
	v_mov_b32_e32 v17, 0
	s_addc_u32 s1, s11, s1
	v_lshl_add_u64 v[18:19], s[0:1], 0, v[16:17]
	s_mov_b64 s[0:1], 0x3810
	s_ashr_i32 s7, s6, 31
	v_lshl_add_u64 v[32:33], v[18:19], 0, s[0:1]
	s_lshl_b64 s[10:11], s[6:7], 12
	s_lshl_b64 s[0:1], s[8:9], 11
	s_add_u32 s0, s2, s0
	v_lshlrev_b32_e32 v16, 4, v20
	s_addc_u32 s1, s3, s1
	v_lshl_add_u64 v[16:17], s[0:1], 0, v[16:17]
	s_mov_b64 s[0:1], 0x4d201c00
	v_lshl_add_u64 v[34:35], v[16:17], 0, s[0:1]
	s_mov_b32 s0, 0x358637bd
	s_lshl_b64 s[12:13], s[6:7], 11
	s_movk_i32 s7, 0xf000
	s_mov_b32 s14, 0x3a800000
	s_mov_b32 s9, 0x800000
	s_movk_i32 s15, 0xd000
	s_movk_i32 s16, 0xe000
	v_mov_b64_e32 v[36:37], s[0:1]
	v_add_co_u32_e32 v42, vcc, 0xfffff000, v34
	s_nop 1
	v_addc_co_u32_e32 v43, vcc, -1, v35, vcc
	global_load_dwordx4 v[140:143], v[34:35], off offset:-2048
	global_load_dwordx4 v[144:147], v[34:35], off offset:-3072
	global_load_dwordx4 v[148:151], v[34:35], off
	global_load_dwordx4 v[152:155], v[34:35], off offset:-1024
	global_load_dwordx4 v[156:159], v[42:43], off offset:-2048
	global_load_dwordx4 v[160:163], v[42:43], off offset:-3072
	global_load_dwordx4 v[164:167], v[42:43], off offset:-1024
	global_load_dwordx4 v[168:171], v[34:35], off offset:-4096
	v_lshl_add_u64 v[34:35], v[34:35], 0, s[12:13]
	s_waitcnt vmcnt(0)
.LBB0_1268:
	v_mov_b64_e32 v[28:29], v[140:141]
	v_mov_b64_e32 v[30:31], v[142:143]
	v_mov_b64_e32 v[24:25], v[144:145]
	v_mov_b64_e32 v[26:27], v[146:147]
	v_mov_b64_e32 v[20:21], v[148:149]
	v_mov_b64_e32 v[22:23], v[150:151]
	v_mov_b64_e32 v[16:17], v[152:153]
	v_mov_b64_e32 v[18:19], v[154:155]
	v_mov_b64_e32 v[46:47], v[156:157]
	v_mov_b64_e32 v[48:49], v[158:159]
	v_mov_b64_e32 v[50:51], v[160:161]
	v_mov_b64_e32 v[52:53], v[162:163]
	v_mov_b64_e32 v[54:55], v[164:165]
	v_mov_b64_e32 v[56:57], v[166:167]
	v_mov_b64_e32 v[58:59], v[168:169]
	v_mov_b64_e32 v[60:61], v[170:171]
	v_add_co_u32_e64 v38, s[0:1], s15, v32
	s_add_i32 s8, s8, s6
	s_nop 0
	v_addc_co_u32_e64 v39, s[0:1], -1, v33, s[0:1]
	v_add_co_u32_e64 v40, s[0:1], s16, v32
	s_cmp_lt_i32 s8, 0x10000
	s_cbranch_scc0 .Lfin_noload
	v_add_co_u32_e32 v42, vcc, 0xfffff000, v34
	s_nop 1
	v_addc_co_u32_e32 v43, vcc, -1, v35, vcc
	global_load_dwordx4 v[140:143], v[34:35], off offset:-2048
	global_load_dwordx4 v[144:147], v[34:35], off offset:-3072
	global_load_dwordx4 v[148:151], v[34:35], off
	global_load_dwordx4 v[152:155], v[34:35], off offset:-1024
	global_load_dwordx4 v[156:159], v[42:43], off offset:-2048
	global_load_dwordx4 v[160:163], v[42:43], off offset:-3072
	global_load_dwordx4 v[164:167], v[42:43], off offset:-1024
	global_load_dwordx4 v[168:171], v[34:35], off offset:-4096
	v_lshl_add_u64 v[34:35], v[34:35], 0, s[12:13]
.Lfin_noload:
	s_nop 0
	v_addc_co_u32_e64 v41, s[0:1], -1, v33, s[0:1]
	v_add_co_u32_e64 v44, s[0:1], s7, v32
	s_nop 0
	v_addc_co_u32_e64 v45, s[0:1], -1, v33, s[0:1]
	v_lshlrev_b32_e32 v43, 16, v28
	v_and_b32_e32 v63, 0xffff0000, v28
	v_and_b32_e32 v62, 0xffff0000, v24
	v_lshlrev_b32_e32 v65, 16, v29
	v_lshlrev_b32_e32 v64, 16, v25
	v_and_b32_e32 v29, 0xffff0000, v29
	v_and_b32_e32 v28, 0xffff0000, v25
	v_lshlrev_b32_e32 v25, 16, v30
	v_and_b32_e32 v67, 0xffff0000, v30
	v_and_b32_e32 v66, 0xffff0000, v26
	v_lshlrev_b32_e32 v69, 16, v31
	v_lshlrev_b32_e32 v68, 16, v27
	v_and_b32_e32 v31, 0xffff0000, v31
	v_and_b32_e32 v30, 0xffff0000, v27
	v_lshlrev_b32_e32 v27, 16, v20
	v_and_b32_e32 v71, 0xffff0000, v20
	v_and_b32_e32 v70, 0xffff0000, v16
	v_lshlrev_b32_e32 v73, 16, v21
	v_lshlrev_b32_e32 v72, 16, v17
	v_and_b32_e32 v21, 0xffff0000, v21
	v_and_b32_e32 v20, 0xffff0000, v17
	v_lshlrev_b32_e32 v17, 16, v22
	v_and_b32_e32 v75, 0xffff0000, v22
	v_and_b32_e32 v74, 0xffff0000, v18
	v_lshlrev_b32_e32 v77, 16, v23
	v_and_b32_e32 v23, 0xffff0000, v23
	v_and_b32_e32 v22, 0xffff0000, v19
	v_lshlrev_b32_e32 v42, 16, v24
	v_lshlrev_b32_e32 v24, 16, v26
	v_lshlrev_b32_e32 v26, 16, v16
	v_lshlrev_b32_e32 v16, 16, v18
	v_lshlrev_b32_e32 v76, 16, v19
	v_pk_mul_f32 v[18:19], v[62:63], v[62:63]
	v_pk_mul_f32 v[78:79], v[28:29], v[28:29]
	v_pk_mul_f32 v[80:81], v[66:67], v[66:67]
	v_pk_mul_f32 v[82:83], v[30:31], v[30:31]
	v_pk_mul_f32 v[84:85], v[70:71], v[70:71]
	v_pk_mul_f32 v[86:87], v[20:21], v[20:21]
	v_pk_mul_f32 v[88:89], v[74:75], v[74:75]
	v_pk_mul_f32 v[90:91], v[22:23], v[22:23]
	v_and_b32_e32 v111, 0xffff0000, v46
	v_and_b32_e32 v110, 0xffff0000, v50
	v_and_b32_e32 v115, 0xffff0000, v47
	v_and_b32_e32 v114, 0xffff0000, v51
	v_and_b32_e32 v117, 0xffff0000, v48
	v_and_b32_e32 v116, 0xffff0000, v52
	v_and_b32_e32 v119, 0xffff0000, v49
	v_and_b32_e32 v118, 0xffff0000, v53
	v_and_b32_e32 v121, 0xffff0000, v58
	v_and_b32_e32 v120, 0xffff0000, v54
; __device__ __forceinline__ float wave_sum(float v) {
;     v += dpp_mov<0xB1>(v);
;     v += dpp_mov<0x4E>(v);
;     v += dpp_mov<0x141>(v);
;     v += dpp_mov<0x140>(v);
;     const float r0 = __builtin_bit_cast(float, __builtin_amdgcn_readlane(__builtin_bit_cast(int, v), 0)), r1 = __builtin_bit_cast(float, __builtin_amdgcn_readlane(__builtin_bit_cast(int, v), 16));
;     const float r2 = __builtin_bit_cast(float, __builtin_amdgcn_readlane(__builtin_bit_cast(int, v), 32)), r3 = __builtin_bit_cast(float, __builtin_amdgcn_readlane(__builtin_bit_cast(int, v), 48));
;     return (r0 + r1) + (r2 + r3);
; __device__ __forceinline__ float ss_u4(const u32x4& v) {
;     const float a = bflo(v.x), b = bfhi(v.x), c = bflo(v.y), d = bfhi(v.y), e = bflo(v.z), f = bfhi(v.z), g = bflo(v.w), h = bfhi(v.w);
;     return ((a * a + b * b) + (c * c + d * d)) + ((e * e + f * f) + (g * g + h * h)); }
; __device__ __forceinline__ void phase_final(const bf16* H, float* out, const float* gain, int gw, int NGW, int lane) {
;     ...
;         for (int r = 0; r < NR; ++r) { const float rstd = rsqrtf(wave_sum(ss_u4(v[r][0]) + ss_u4(v[r][1])) * (1.f / DM) + EPS);
	v_and_b32_e32 v123, 0xffff0000, v59
	v_and_b32_e32 v122, 0xffff0000, v55
	v_and_b32_e32 v125, 0xffff0000, v60
	v_and_b32_e32 v124, 0xffff0000, v56
	v_and_b32_e32 v127, 0xffff0000, v61
	v_and_b32_e32 v126, 0xffff0000, v57
	v_mov_b32_e32 v92, v42
	v_mov_b32_e32 v93, v62
	v_mov_b32_e32 v94, v64
	v_mov_b32_e32 v95, v28
	v_mov_b32_e32 v96, v24
	v_mov_b32_e32 v97, v66
	v_mov_b32_e32 v98, v68
	v_mov_b32_e32 v99, v30
	v_mov_b32_e32 v62, v43
	v_mov_b32_e32 v28, v65
	v_mov_b32_e32 v66, v25
	v_mov_b32_e32 v30, v69
	v_mov_b32_e32 v100, v26
	v_mov_b32_e32 v101, v70
	v_mov_b32_e32 v102, v72
	v_mov_b32_e32 v103, v20
	v_mov_b32_e32 v104, v16
	v_mov_b32_e32 v105, v74
	v_mov_b32_e32 v106, v76
	v_mov_b32_e32 v107, v22
	v_mov_b32_e32 v70, v27
	v_mov_b32_e32 v20, v73
	v_mov_b32_e32 v74, v17
	v_mov_b32_e32 v22, v77
	v_lshlrev_b32_e32 v109, 16, v46
	v_lshlrev_b32_e32 v108, 16, v50
	v_lshlrev_b32_e32 v113, 16, v47
	v_lshlrev_b32_e32 v112, 16, v51
	v_lshlrev_b32_e32 v47, 16, v48
	v_lshlrev_b32_e32 v46, 16, v52
	v_lshlrev_b32_e32 v51, 16, v49
	v_lshlrev_b32_e32 v50, 16, v53
	v_lshlrev_b32_e32 v48, 16, v54
	v_lshlrev_b32_e32 v49, 16, v58
	v_lshlrev_b32_e32 v52, 16, v55
	v_lshlrev_b32_e32 v53, 16, v59
	v_lshlrev_b32_e32 v54, 16, v56
	v_lshlrev_b32_e32 v55, 16, v60
	v_lshlrev_b32_e32 v58, 16, v57
	v_lshlrev_b32_e32 v59, 16, v61
	v_pk_fma_f32 v[18:19], v[42:43], v[42:43], v[18:19]
	v_pk_fma_f32 v[42:43], v[64:65], v[64:65], v[78:79]
	v_pk_fma_f32 v[24:25], v[24:25], v[24:25], v[80:81]
	v_pk_fma_f32 v[56:57], v[68:69], v[68:69], v[82:83]
	v_pk_fma_f32 v[26:27], v[26:27], v[26:27], v[84:85]
	v_pk_fma_f32 v[60:61], v[72:73], v[72:73], v[86:87]
	v_pk_fma_f32 v[16:17], v[16:17], v[16:17], v[88:89]
	v_pk_fma_f32 v[64:65], v[76:77], v[76:77], v[90:91]
	v_pk_mul_f32 v[68:69], v[110:111], v[110:111]
	v_pk_mul_f32 v[72:73], v[114:115], v[114:115]
	v_pk_mul_f32 v[76:77], v[116:117], v[116:117]
	v_pk_mul_f32 v[78:79], v[118:119], v[118:119]
	v_pk_mul_f32 v[80:81], v[120:121], v[120:121]
	v_pk_mul_f32 v[82:83], v[122:123], v[122:123]
	v_pk_mul_f32 v[84:85], v[124:125], v[124:125]
	v_pk_mul_f32 v[86:87], v[126:127], v[126:127]
	v_mov_b32_e32 v128, v46
	v_mov_b32_e32 v129, v116
	v_mov_b32_e32 v130, v50
	v_mov_b32_e32 v131, v118
	v_mov_b32_e32 v116, v47
	v_mov_b32_e32 v118, v51
	v_mov_b32_e32 v132, v48
	v_mov_b32_e32 v133, v120
	v_mov_b32_e32 v134, v52
	v_mov_b32_e32 v135, v122
	v_mov_b32_e32 v136, v54
	v_mov_b32_e32 v137, v124
	v_mov_b32_e32 v138, v58
	v_mov_b32_e32 v139, v126
	v_mov_b32_e32 v120, v49
	v_mov_b32_e32 v122, v53
	v_mov_b32_e32 v124, v55
	v_mov_b32_e32 v126, v59
	v_pk_add_f32 v[18:19], v[18:19], v[42:43]
	v_pk_add_f32 v[24:25], v[24:25], v[56:57]
	v_pk_add_f32 v[26:27], v[26:27], v[60:61]
	v_pk_add_f32 v[16:17], v[16:17], v[64:65]
	v_pk_fma_f32 v[42:43], v[108:109], v[108:109], v[68:69]
	v_pk_fma_f32 v[56:57], v[112:113], v[112:113], v[72:73]
	v_pk_fma_f32 v[46:47], v[46:47], v[46:47], v[76:77]
	v_pk_fma_f32 v[50:51], v[50:51], v[50:51], v[78:79]
	v_pk_fma_f32 v[48:49], v[48:49], v[48:49], v[80:81]
	v_pk_fma_f32 v[52:53], v[52:53], v[52:53], v[82:83]
	v_pk_fma_f32 v[54:55], v[54:55], v[54:55], v[84:85]
	v_pk_fma_f32 v[58:59], v[58:59], v[58:59], v[86:87]
	v_pk_add_f32 v[18:19], v[18:19], v[24:25]
	v_pk_add_f32 v[16:17], v[26:27], v[16:17]
	v_pk_add_f32 v[24:25], v[42:43], v[56:57]
	v_pk_add_f32 v[26:27], v[46:47], v[50:51]
	v_pk_add_f32 v[42:43], v[48:49], v[52:53]
	v_pk_add_f32 v[46:47], v[54:55], v[58:59]
	v_add_f32_e32 v48, v18, v19
	v_add_f32_e32 v49, v16, v17
	v_pk_add_f32 v[16:17], v[24:25], v[26:27]
	v_pk_add_f32 v[18:19], v[42:43], v[46:47]
	v_add_f32_dpp v24, v48, v48 quad_perm:[1,0,3,2] row_mask:0xf bank_mask:0xf bound_ctrl:1
	v_add_f32_dpp v25, v49, v49 quad_perm:[1,0,3,2] row_mask:0xf bank_mask:0xf bound_ctrl:1
	v_add_f32_e32 v16, v16, v17
	v_add_f32_e32 v17, v18, v19
	v_add_f32_dpp v18, v24, v24 quad_perm:[2,3,0,1] row_mask:0xf bank_mask:0xf bound_ctrl:1
	v_add_f32_dpp v19, v25, v25 quad_perm:[2,3,0,1] row_mask:0xf bank_mask:0xf bound_ctrl:1
	v_add_f32_dpp v16, v16, v16 quad_perm:[1,0,3,2] row_mask:0xf bank_mask:0xf bound_ctrl:1
	v_add_f32_dpp v17, v17, v17 quad_perm:[1,0,3,2] row_mask:0xf bank_mask:0xf bound_ctrl:1
	v_add_f32_dpp v18, v18, v18 row_half_mirror row_mask:0xf bank_mask:0xf bound_ctrl:1
	v_add_f32_dpp v19, v19, v19 row_half_mirror row_mask:0xf bank_mask:0xf bound_ctrl:1
	v_add_f32_dpp v16, v16, v16 quad_perm:[2,3,0,1] row_mask:0xf bank_mask:0xf bound_ctrl:1
	v_add_f32_dpp v17, v17, v17 quad_perm:[2,3,0,1] row_mask:0xf bank_mask:0xf bound_ctrl:1
	v_add_f32_dpp v18, v18, v18 row_mirror row_mask:0xf bank_mask:0xf bound_ctrl:1
	v_add_f32_dpp v19, v19, v19 row_mirror row_mask:0xf bank_mask:0xf bound_ctrl:1
	v_add_f32_dpp v16, v16, v16 row_half_mirror row_mask:0xf bank_mask:0xf bound_ctrl:1
	v_add_f32_dpp v17, v17, v17 row_half_mirror row_mask:0xf bank_mask:0xf bound_ctrl:1
	v_readlane_b32 s4, v18, 16
	v_readlane_b32 s5, v18, 48
	v_readlane_b32 s17, v19, 16
	v_readlane_b32 s18, v19, 48
	v_add_f32_dpp v24, v16, v16 row_mirror row_mask:0xf bank_mask:0xf bound_ctrl:1
	v_add_f32_dpp v25, v17, v17 row_mirror row_mask:0xf bank_mask:0xf bound_ctrl:1
	v_readlane_b32 s0, v18, 0
	v_readlane_b32 s1, v18, 32
	v_readlane_b32 s2, v19, 0
	v_readlane_b32 s3, v19, 32
	v_mov_b32_e32 v16, s4
	v_mov_b32_e32 v17, s5
	v_mov_b32_e32 v18, s17
	v_mov_b32_e32 v19, s18
	v_readlane_b32 s17, v24, 16
	v_readlane_b32 s20, v24, 48
	v_readlane_b32 s21, v25, 16
	v_readlane_b32 s22, v25, 48
	v_readlane_b32 s4, v24, 0
	v_readlane_b32 s5, v24, 32
	v_readlane_b32 s18, v25, 0
	v_readlane_b32 s19, v25, 32
	v_pk_add_f32 v[16:17], s[0:1], v[16:17]
	v_pk_add_f32 v[18:19], s[2:3], v[18:19]
; __device__ __forceinline__ void phase_final(const bf16* H, float* out, const float* gain, int gw, int NGW, int lane) {
;     ...
;         for (int r = 0; r < NR; ++r) { const float rstd = rsqrtf(wave_sum(ss_u4(v[r][0]) + ss_u4(v[r][1])) * (1.f / DM) + EPS);
;             f32x4* xr = (f32x4*)(out + (size_t)(m0 + r) * DM);
; #pragma unroll
;             for (int j = 0; j < 2; ++j) { const u32x4 w = v[r][j];
;                 xr[2 * lane + 128 * j] = (f32x4){bflo(w.x), bfhi(w.x), bflo(w.y), bfhi(w.y)} * rstd * gv[j][0];
;                 xr[2 * lane + 128 * j + 1] = (f32x4){bflo(w.z), bfhi(w.z), bflo(w.w), bfhi(w.w)} * rstd * gv[j][1]; } } }
	v_mov_b32_e32 v24, s17
	v_mov_b32_e32 v25, s20
	v_mov_b32_e32 v26, s21
	v_mov_b32_e32 v27, s22
	v_mov_b32_e32 v42, v18
	v_mov_b32_e32 v43, v16
	v_mov_b32_e32 v16, v19
	v_pk_add_f32 v[18:19], s[4:5], v[24:25]
	v_pk_add_f32 v[24:25], s[18:19], v[26:27]
	v_pk_add_f32 v[16:17], v[42:43], v[16:17]
	v_mov_b32_e32 v26, v24
	v_mov_b32_e32 v27, v18
	v_mov_b32_e32 v18, v25
	v_pk_fma_f32 v[16:17], v[16:17], s[14:15], v[36:37] op_sel_hi:[1,0,0]
	v_pk_add_f32 v[18:19], v[26:27], v[18:19]
	v_mul_f32_e32 v24, 0x4b800000, v17
	v_mul_f32_e32 v25, 0x4b800000, v16
	v_cmp_gt_f32_e32 vcc, s9, v16
	v_cmp_gt_f32_e64 s[0:1], s9, v17
	v_pk_fma_f32 v[18:19], v[18:19], s[14:15], v[36:37] op_sel_hi:[1,0,0]
	v_cndmask_b32_e32 v16, v16, v25, vcc
	v_cndmask_b32_e64 v17, v17, v24, s[0:1]
	v_mul_f32_e32 v24, 0x4b800000, v19
	v_cmp_gt_f32_e64 s[4:5], s9, v19
	v_mul_f32_e32 v25, 0x4b800000, v18
	v_cmp_gt_f32_e64 s[2:3], s9, v18
	v_rsq_f32_e32 v17, v17
	v_rsq_f32_e32 v26, v16
	v_cndmask_b32_e64 v16, v19, v24, s[4:5]
	v_cndmask_b32_e64 v18, v18, v25, s[2:3]
	v_rsq_f32_e32 v19, v16
	v_rsq_f32_e32 v69, v18
	v_mul_f32_e32 v16, 0x45800000, v17
	v_mul_f32_e32 v18, 0x45800000, v26
	v_cndmask_b32_e64 v16, v17, v16, s[0:1]
	v_cndmask_b32_e32 v18, v26, v18, vcc
	v_mul_f32_e32 v17, 0x45800000, v19
	v_mov_b32_e32 v88, v108
	v_mov_b32_e32 v89, v110
	v_mov_b32_e32 v90, v112
	v_mov_b32_e32 v91, v114
	v_mul_f32_e32 v72, 0x45800000, v69
	v_pk_mul_f32 v[24:25], v[16:17], v[92:93] op_sel_hi:[0,1]
	v_pk_mul_f32 v[26:27], v[16:17], v[94:95] op_sel_hi:[0,1]
	v_pk_mul_f32 v[42:43], v[16:17], v[96:97] op_sel_hi:[0,1]
	v_pk_mul_f32 v[48:49], v[16:17], v[62:63] op_sel_hi:[0,1]
	v_pk_mul_f32 v[28:29], v[16:17], v[28:29] op_sel_hi:[0,1]
	v_pk_mul_f32 v[50:51], v[16:17], v[66:67] op_sel_hi:[0,1]
	v_pk_mul_f32 v[56:57], v[18:19], v[104:105] op_sel_hi:[0,1]
	v_pk_mul_f32 v[62:63], v[18:19], v[20:21] op_sel_hi:[0,1]
	v_cndmask_b32_e64 v68, v19, v17, s[4:5]
	v_mov_b32_e32 v110, v109
	v_mov_b32_e32 v114, v113
	v_pk_mul_f32 v[46:47], v[16:17], v[98:99] op_sel_hi:[0,1]
	v_pk_mul_f32 v[30:31], v[16:17], v[30:31] op_sel_hi:[0,1]
	v_pk_mul_f32 v[52:53], v[18:19], v[100:101] op_sel_hi:[0,1]
	v_pk_mul_f32 v[54:55], v[18:19], v[102:103] op_sel_hi:[0,1]
	v_pk_mul_f32 v[58:59], v[18:19], v[106:107] op_sel_hi:[0,1]
	v_pk_mul_f32 v[60:61], v[18:19], v[70:71] op_sel_hi:[0,1]
	v_pk_mul_f32 v[64:65], v[18:19], v[74:75] op_sel_hi:[0,1]
	v_pk_mul_f32 v[66:67], v[18:19], v[22:23] op_sel_hi:[0,1]
	v_cndmask_b32_e64 v70, v69, v72, s[2:3]
	v_pk_mul_f32 v[18:19], v[6:7], v[26:27]
	v_pk_mul_f32 v[16:17], v[4:5], v[24:25]
	v_pk_mul_f32 v[20:21], v[0:1], v[42:43]
	v_pk_mul_f32 v[26:27], v[14:15], v[28:29]
	v_pk_mul_f32 v[28:29], v[8:9], v[50:51]
	v_pk_mul_f32 v[50:51], v[0:1], v[56:57]
	v_pk_mul_f32 v[56:57], v[14:15], v[62:63]
	v_pk_mul_f32 v[42:43], v[68:69], v[88:89] op_sel_hi:[0,1]
	v_pk_mul_f32 v[62:63], v[68:69], v[90:91] op_sel_hi:[0,1]
	v_pk_mul_f32 v[22:23], v[2:3], v[46:47]
	v_pk_mul_f32 v[24:25], v[12:13], v[48:49]
	v_pk_mul_f32 v[30:31], v[10:11], v[30:31]
	v_pk_mul_f32 v[48:49], v[6:7], v[54:55]
	v_pk_mul_f32 v[46:47], v[4:5], v[52:53]
	v_pk_mul_f32 v[52:53], v[2:3], v[58:59]
	v_pk_mul_f32 v[54:55], v[12:13], v[60:61]
	v_pk_mul_f32 v[60:61], v[10:11], v[66:67]
	v_pk_mul_f32 v[58:59], v[8:9], v[64:65]
	v_pk_mul_f32 v[64:65], v[68:69], v[128:129] op_sel_hi:[0,1]
	v_pk_mul_f32 v[66:67], v[68:69], v[130:131] op_sel_hi:[0,1]
	v_pk_mul_f32 v[72:73], v[68:69], v[110:111] op_sel_hi:[0,1]
	v_pk_mul_f32 v[74:75], v[68:69], v[114:115] op_sel_hi:[0,1]
	v_pk_mul_f32 v[76:77], v[68:69], v[116:117] op_sel_hi:[0,1]
	v_pk_mul_f32 v[68:69], v[68:69], v[118:119] op_sel_hi:[0,1]
	v_pk_mul_f32 v[78:79], v[70:71], v[132:133] op_sel_hi:[0,1]
	v_pk_mul_f32 v[80:81], v[70:71], v[134:135] op_sel_hi:[0,1]
	v_pk_mul_f32 v[82:83], v[70:71], v[136:137] op_sel_hi:[0,1]
	v_pk_mul_f32 v[84:85], v[70:71], v[138:139] op_sel_hi:[0,1]
	v_pk_mul_f32 v[86:87], v[70:71], v[120:121] op_sel_hi:[0,1]
	v_pk_mul_f32 v[88:89], v[70:71], v[122:123] op_sel_hi:[0,1]
	v_pk_mul_f32 v[90:91], v[70:71], v[124:125] op_sel_hi:[0,1]
	v_pk_mul_f32 v[70:71], v[70:71], v[126:127] op_sel_hi:[0,1]
	global_store_dwordx4 v[44:45], v[16:19], off offset:-2064
	global_store_dwordx4 v[44:45], v[20:23], off offset:-2048
	global_store_dwordx4 v[44:45], v[24:27], off offset:-16
	global_store_dwordx4 v[32:33], v[28:31], off offset:-4096
	global_store_dwordx4 v[32:33], v[46:49], off offset:-2064
	global_store_dwordx4 v[32:33], v[50:53], off offset:-2048
	global_store_dwordx4 v[32:33], v[54:57], off offset:-16
	global_store_dwordx4 v[32:33], v[58:61], off
	v_lshl_add_u64 v[32:33], v[32:33], 0, s[10:11]
	v_pk_mul_f32 v[18:19], v[6:7], v[62:63]
	v_pk_mul_f32 v[16:17], v[4:5], v[42:43]
	v_pk_mul_f32 v[22:23], v[2:3], v[66:67]
	v_pk_mul_f32 v[20:21], v[0:1], v[64:65]
	v_pk_mul_f32 v[26:27], v[14:15], v[74:75]
	v_pk_mul_f32 v[24:25], v[12:13], v[72:73]
	v_pk_mul_f32 v[30:31], v[10:11], v[68:69]
	v_pk_mul_f32 v[28:29], v[8:9], v[76:77]
	v_pk_mul_f32 v[44:45], v[6:7], v[80:81]
	v_pk_mul_f32 v[42:43], v[4:5], v[78:79]
	v_pk_mul_f32 v[48:49], v[2:3], v[84:85]
	v_pk_mul_f32 v[46:47], v[0:1], v[82:83]
	v_pk_mul_f32 v[52:53], v[14:15], v[88:89]
	v_pk_mul_f32 v[50:51], v[12:13], v[86:87]
	v_pk_mul_f32 v[56:57], v[10:11], v[70:71]
	v_pk_mul_f32 v[54:55], v[8:9], v[90:91]
	global_store_dwordx4 v[38:39], v[16:19], off offset:-2064
	global_store_dwordx4 v[38:39], v[20:23], off offset:-2048
	global_store_dwordx4 v[38:39], v[24:27], off offset:-16
	global_store_dwordx4 v[40:41], v[28:31], off offset:-4096
	global_store_dwordx4 v[40:41], v[42:45], off offset:-2064
	global_store_dwordx4 v[40:41], v[46:49], off offset:-2048
	global_store_dwordx4 v[40:41], v[50:53], off offset:-16
	global_store_dwordx4 v[40:41], v[54:57], off
	s_waitcnt vmcnt(16)
	s_cbranch_scc1 .LBB0_1268
